# baseline (speedup 1.0000x reference)
.Lit7b:
	global_load_dwordx4 v[112:115], v164, s[24:25]
	v_mfma_f32_16x16x32_f16 v[120:123], v[16:19], v[116:119], 0
	v_mfma_f32_16x16x32_f16 v[124:127], v[20:23], v[116:119], 0
	v_cndmask_b32_e32 v158, 4, v158, vcc
	v_mfma_f32_16x16x32_f16 v[128:131], v[24:27], v[116:119], 0
	v_mfma_f32_16x16x32_f16 v[132:135], v[28:31], v[116:119], 0
	v_min3_i32 v160, v136, v137, v157
	v_min3_i32 v160, v138, v139, v160
	v_min3_i32 v160, v140, v141, v160
	v_min3_i32 v160, v142, v143, v160
	v_min3_i32 v160, v144, v145, v160
	v_min3_i32 v160, v146, v147, v160
	v_min3_i32 v160, v148, v149, v160
	v_min3_i32 v156, v150, v151, v160
	v_cmp_ge_i32_e32 vcc, v156, v157
	v_mfma_f32_16x16x32_f16 v[136:139], v[32:35], v[116:119], 0
	v_mfma_f32_16x16x32_f16 v[140:143], v[36:39], v[116:119], 0
	v_cndmask_b32_e32 v158, 5, v158, vcc
	v_add_u32_e32 v162, s40, v158
	v_lshl_or_b32 v162, v162, 2, v166
	v_mov_b32_e32 v163, v156
	ds_min_u64 v167, v[162:163] offset:17152
	v_mfma_f32_16x16x32_f16 v[144:147], v[40:43], v[116:119], 0
	v_mfma_f32_16x16x32_f16 v[148:151], v[44:47], v[116:119], 0
	v_min3_i32 v160, v120, v121, s41
	v_min3_i32 v160, v122, v123, v160
	v_min3_i32 v160, v124, v125, v160
	v_min3_i32 v160, v126, v127, v160
	v_min3_i32 v160, v128, v129, v160
	v_min3_i32 v160, v130, v131, v160
	v_min3_i32 v160, v132, v133, v160
	v_min3_i32 v157, v134, v135, v160
	v_mfma_f32_16x16x32_f16 v[120:123], v[48:51], v[116:119], 0
	v_mfma_f32_16x16x32_f16 v[124:127], v[52:55], v[116:119], 0
	v_mov_b32_e32 v158, 0
	v_mfma_f32_16x16x32_f16 v[128:131], v[56:59], v[116:119], 0
	v_mfma_f32_16x16x32_f16 v[132:135], v[60:63], v[116:119], 0
	v_min3_i32 v160, v136, v137, v157
	v_min3_i32 v160, v138, v139, v160
	v_min3_i32 v160, v140, v141, v160
	v_min3_i32 v160, v142, v143, v160
	v_min3_i32 v160, v144, v145, v160
	v_min3_i32 v160, v146, v147, v160
	v_min3_i32 v160, v148, v149, v160
	v_min3_i32 v156, v150, v151, v160
	v_cmp_ge_i32_e32 vcc, v156, v157
	v_mfma_f32_16x16x32_f16 v[136:139], v[64:67], v[116:119], 0
	v_mfma_f32_16x16x32_f16 v[140:143], v[68:71], v[116:119], 0
	v_cndmask_b32_e32 v158, 1, v158, vcc
	v_mfma_f32_16x16x32_f16 v[144:147], v[72:75], v[116:119], 0
	v_mfma_f32_16x16x32_f16 v[148:151], v[76:79], v[116:119], 0
	v_min3_i32 v160, v120, v121, v156
	v_min3_i32 v160, v122, v123, v160
	v_min3_i32 v160, v124, v125, v160
	v_min3_i32 v160, v126, v127, v160
	v_min3_i32 v160, v128, v129, v160
	v_min3_i32 v160, v130, v131, v160
	v_min3_i32 v160, v132, v133, v160
	v_min3_i32 v157, v134, v135, v160
	v_cmp_ge_i32_e32 vcc, v157, v156
	v_mfma_f32_16x16x32_f16 v[120:123], v[80:83], v[116:119], 0
	v_mfma_f32_16x16x32_f16 v[124:127], v[84:87], v[116:119], 0
	v_cndmask_b32_e32 v158, 2, v158, vcc
	v_mfma_f32_16x16x32_f16 v[128:131], v[88:91], v[116:119], 0
	v_mfma_f32_16x16x32_f16 v[132:135], v[92:95], v[116:119], 0
	v_min3_i32 v160, v136, v137, v157
	v_min3_i32 v160, v138, v139, v160
	v_min3_i32 v160, v140, v141, v160
	v_min3_i32 v160, v142, v143, v160
	v_min3_i32 v160, v144, v145, v160
	v_min3_i32 v160, v146, v147, v160
	v_min3_i32 v160, v148, v149, v160
	v_min3_i32 v156, v150, v151, v160
	v_cmp_ge_i32_e32 vcc, v156, v157
	v_mfma_f32_16x16x32_f16 v[136:139], v[96:99], v[116:119], 0
	v_mfma_f32_16x16x32_f16 v[140:143], v[100:103], v[116:119], 0
	v_cndmask_b32_e32 v158, 3, v158, vcc
	v_mfma_f32_16x16x32_f16 v[144:147], v[104:107], v[116:119], 0
	v_mfma_f32_16x16x32_f16 v[148:151], v[108:111], v[116:119], 0
	v_min3_i32 v160, v120, v121, v156
	v_min3_i32 v160, v122, v123, v160
	v_min3_i32 v160, v124, v125, v160
	v_min3_i32 v160, v126, v127, v160
	v_min3_i32 v160, v128, v129, v160
	v_min3_i32 v160, v130, v131, v160
	v_min3_i32 v160, v132, v133, v160
	v_min3_i32 v157, v134, v135, v160
	v_cmp_ge_i32_e32 vcc, v157, v156
	s_waitcnt vmcnt(0)
	v_mfma_f32_16x16x32_f16 v[120:123], v[16:19], v[112:115], 0
	v_mfma_f32_16x16x32_f16 v[124:127], v[20:23], v[112:115], 0
	v_cndmask_b32_e32 v158, 4, v158, vcc
	v_mfma_f32_16x16x32_f16 v[128:131], v[24:27], v[112:115], 0
	v_mfma_f32_16x16x32_f16 v[132:135], v[28:31], v[112:115], 0
	v_min3_i32 v160, v136, v137, v157
	v_min3_i32 v160, v138, v139, v160
	v_min3_i32 v160, v140, v141, v160
	v_min3_i32 v160, v142, v143, v160
	v_min3_i32 v160, v144, v145, v160
	v_min3_i32 v160, v146, v147, v160
	v_min3_i32 v160, v148, v149, v160
	v_min3_i32 v156, v150, v151, v160
	v_cmp_ge_i32_e32 vcc, v156, v157
	v_mfma_f32_16x16x32_f16 v[136:139], v[32:35], v[112:115], 0
	v_mfma_f32_16x16x32_f16 v[140:143], v[36:39], v[112:115], 0
	v_cndmask_b32_e32 v158, 5, v158, vcc
	v_add_u32_e32 v162, s40, v158
	v_lshl_or_b32 v162, v162, 2, v166
	v_mov_b32_e32 v163, v156
	ds_min_u64 v167, v[162:163] offset:17280
	v_mfma_f32_16x16x32_f16 v[144:147], v[40:43], v[112:115], 0
	v_mfma_f32_16x16x32_f16 v[148:151], v[44:47], v[112:115], 0
	v_min3_i32 v160, v120, v121, s41
	v_min3_i32 v160, v122, v123, v160
	v_min3_i32 v160, v124, v125, v160
	v_min3_i32 v160, v126, v127, v160
	v_min3_i32 v160, v128, v129, v160
	v_min3_i32 v160, v130, v131, v160
	v_min3_i32 v160, v132, v133, v160
	v_min3_i32 v157, v134, v135, v160
	v_mfma_f32_16x16x32_f16 v[120:123], v[48:51], v[112:115], 0
	v_mfma_f32_16x16x32_f16 v[124:127], v[52:55], v[112:115], 0
	v_mov_b32_e32 v158, 0
	v_mfma_f32_16x16x32_f16 v[128:131], v[56:59], v[112:115], 0
	v_mfma_f32_16x16x32_f16 v[132:135], v[60:63], v[112:115], 0
	v_min3_i32 v160, v136, v137, v157
	v_min3_i32 v160, v138, v139, v160
	v_min3_i32 v160, v140, v141, v160
	v_min3_i32 v160, v142, v143, v160
	v_min3_i32 v160, v144, v145, v160
	v_min3_i32 v160, v146, v147, v160
	v_min3_i32 v160, v148, v149, v160
	v_min3_i32 v156, v150, v151, v160
	v_cmp_ge_i32_e32 vcc, v156, v157
	v_mfma_f32_16x16x32_f16 v[136:139], v[64:67], v[112:115], 0
	v_mfma_f32_16x16x32_f16 v[140:143], v[68:71], v[112:115], 0
	v_cndmask_b32_e32 v158, 1, v158, vcc
	v_mfma_f32_16x16x32_f16 v[144:147], v[72:75], v[112:115], 0
	v_mfma_f32_16x16x32_f16 v[148:151], v[76:79], v[112:115], 0
	v_min3_i32 v160, v120, v121, v156
	v_min3_i32 v160, v122, v123, v160
	v_min3_i32 v160, v124, v125, v160
	v_min3_i32 v160, v126, v127, v160
	v_min3_i32 v160, v128, v129, v160
	v_min3_i32 v160, v130, v131, v160
	v_min3_i32 v160, v132, v133, v160
	v_min3_i32 v157, v134, v135, v160
	v_cmp_ge_i32_e32 vcc, v157, v156
	v_mfma_f32_16x16x32_f16 v[120:123], v[80:83], v[112:115], 0
	v_mfma_f32_16x16x32_f16 v[124:127], v[84:87], v[112:115], 0
	v_cndmask_b32_e32 v158, 2, v158, vcc
	v_mfma_f32_16x16x32_f16 v[128:131], v[88:91], v[112:115], 0
	v_mfma_f32_16x16x32_f16 v[132:135], v[92:95], v[112:115], 0
	v_min3_i32 v160, v136, v137, v157
	v_min3_i32 v160, v138, v139, v160
	v_min3_i32 v160, v140, v141, v160
	v_min3_i32 v160, v142, v143, v160
	v_min3_i32 v160, v144, v145, v160
	v_min3_i32 v160, v146, v147, v160
	v_min3_i32 v160, v148, v149, v160
	v_min3_i32 v156, v150, v151, v160
	v_cmp_ge_i32_e32 vcc, v156, v157
	v_mfma_f32_16x16x32_f16 v[136:139], v[96:99], v[112:115], 0
	v_mfma_f32_16x16x32_f16 v[140:143], v[100:103], v[112:115], 0
	v_cndmask_b32_e32 v158, 3, v158, vcc
	v_mfma_f32_16x16x32_f16 v[144:147], v[104:107], v[112:115], 0
	v_mfma_f32_16x16x32_f16 v[148:151], v[108:111], v[112:115], 0
	v_min3_i32 v160, v120, v121, v156
	v_min3_i32 v160, v122, v123, v160
	v_min3_i32 v160, v124, v125, v160
	v_min3_i32 v160, v126, v127, v160
	v_min3_i32 v160, v128, v129, v160
	v_min3_i32 v160, v130, v131, v160
	v_min3_i32 v160, v132, v133, v160
	v_min3_i32 v157, v134, v135, v160
	v_cmp_ge_i32_e32 vcc, v157, v156
	s_nop 1
	v_cndmask_b32_e32 v158, 4, v158, vcc
	s_nop 7
	v_min3_i32 v160, v136, v137, v157
	v_min3_i32 v160, v138, v139, v160
	v_min3_i32 v160, v140, v141, v160
	v_min3_i32 v160, v142, v143, v160
	v_min3_i32 v160, v144, v145, v160
	v_min3_i32 v160, v146, v147, v160
	v_min3_i32 v160, v148, v149, v160
	v_min3_i32 v156, v150, v151, v160
	v_cmp_ge_i32_e32 vcc, v156, v157
	s_nop 1
	v_cndmask_b32_e32 v158, 5, v158, vcc
	v_add_u32_e32 v162, s40, v158
	v_lshl_or_b32 v162, v162, 2, v166
	v_mov_b32_e32 v163, v156
	ds_min_u64 v167, v[162:163] offset:17408
	s_waitcnt lgkmcnt(0)
	s_barrier
	s_setprio 0
	s_cmp_eq_u32 s50, 0
	s_cbranch_scc0 .Lprio2_done
	s_setprio 2
.Lprio2_done:
	s_add_i32 s65, s50, 4
	s_mov_b32 s66, 8
	s_cmp_ge_u32 s50, 2
	s_cbranch_scc0 .Lq1
	s_lshl_b32 s60, s65, 7
	v_add_u32_e32 v2, s60, v169
	ds_read_b32 v216, v2 offset:16384
	s_lshl_b32 s60, s65, 10
	v_add_u32_e32 v248, s60, v170
